# baseline (speedup 1.0000x reference)
.LBB3_35:
.LBB3_36:
.LBB3_37:
.LBB3_38:
.LBB3_39:
	s_and_b64 vcc, exec, s[28:29]
	s_cbranch_vccz .L39_full
	v_sub_u32_e32 v20, 0x7f000000, v2
	s_branch .L39_tail

.L39_tail:
	s_sub_i32 s34, 0xe0, s3
	s_mul_i32 s35, s34, 33
	s_mul_i32 s36, s3, 0x210
	v_mov_b32_e32 v104, 0
	v_mov_b32_e32 v105, 0
	v_mov_b32_e32 v106, 0
	v_mov_b32_e32 v107, 0
	v_mov_b32_e32 v108, v0
	v_lshlrev_b32_e32 v109, 4, v0
	v_add_u32_e32 v109, s36, v109
	s_mov_b64 s[36:37], exec

.Lz_done:
	s_mov_b64 exec, s[36:37]
	v_cmp_gt_u32_e32 vcc, s34, v0
	v_add_u32_e32 v109, s3, v0
	v_lshlrev_b32_e32 v109, 2, v109
	v_add_u32_e32 v109, 0x22200, v109
	s_and_saveexec_b64 s[36:37], vcc
	ds_write_b32 v109, v104
	s_mov_b64 exec, s[36:37]
	s_waitcnt lgkmcnt(0)
	s_barrier
	s_and_b64 vcc, exec, s[28:29]
	s_cbranch_vccz .LBB3_43
	v_sub_u32_e32 v103, 0x7f000000, v20
	s_waitcnt vmcnt(0)
	v_cvt_pk_f16_f32 v64, v64, v65
	v_mul_f32_e32 v66, v103, v66
	v_cvt_pk_f16_f32 v65, v66, 0
	v_mov_b32_e32 v66, 0
	v_mov_b32_e32 v67, 0
	v_cvt_pk_f16_f32 v68, v68, v69
	v_mul_f32_e32 v70, v103, v70
	v_cvt_pk_f16_f32 v69, v70, 0
	v_mov_b32_e32 v70, 0
	v_mov_b32_e32 v71, 0
	v_cvt_pk_f16_f32 v72, v72, v73
	v_mul_f32_e32 v74, v103, v74
	v_cvt_pk_f16_f32 v73, v74, 0
	v_mov_b32_e32 v74, 0
	v_mov_b32_e32 v75, 0
	v_cvt_pk_f16_f32 v76, v76, v77
	v_mul_f32_e32 v78, v103, v78
	v_cvt_pk_f16_f32 v77, v78, 0
	v_mov_b32_e32 v78, 0
	v_mov_b32_e32 v79, 0
	v_cvt_pk_f16_f32 v80, v80, v81
	v_mul_f32_e32 v82, v103, v82
	v_cvt_pk_f16_f32 v81, v82, 0
	v_mov_b32_e32 v82, 0
	v_mov_b32_e32 v83, 0
	v_cvt_pk_f16_f32 v84, v84, v85
	v_mul_f32_e32 v86, v103, v86
	v_cvt_pk_f16_f32 v85, v86, 0
	v_mov_b32_e32 v86, 0
	v_mov_b32_e32 v87, 0
	v_cvt_pk_f16_f32 v88, v88, v89
	v_mul_f32_e32 v90, v103, v90
	v_cvt_pk_f16_f32 v89, v90, 0
	v_mov_b32_e32 v90, 0
	v_mov_b32_e32 v91, 0
	v_cvt_pk_f16_f32 v92, v92, v93
	v_mul_f32_e32 v94, v103, v94
	v_cvt_pk_f16_f32 v93, v94, 0
	v_mov_b32_e32 v94, 0
	v_mov_b32_e32 v95, 0
	v_mov_b32_e32 v34, 0
	v_mov_b32_e32 v35, 0
	v_mov_b32_e32 v40, 0
	v_mov_b32_e32 v41, 0
	v_add_u32_e32 v14, 3, v96
	v_lshrrev_b32_e32 v14, 2, v14
	v_add_u32_e32 v15, v97, v14
	v_add_u32_e32 v16, v97, v99
	v_mov_b32_e32 v13, 0x1ce00
	s_mov_b64 s[58:59], exec
